# baseline (speedup 1.0000x reference)
.Lfl_priv:
	s_cmp_eq_u32 s3, 0
	s_cbranch_scc1 .LBB1_104
	s_waitcnt lgkmcnt(0)
	v_and_b32_e32 v77, 1, v76
	v_cmp_ne_u32_e32 vcc, 0, v77
	s_and_b64 exec, exec, vcc
	global_store_dwordx4 v42, v[44:47], s[14:15]
	s_mov_b64 exec, -1
	v_and_b32_e32 v77, 4, v76
	v_cmp_ne_u32_e32 vcc, 0, v77
	s_and_b64 exec, exec, vcc
	global_store_dwordx4 v42, v[48:51], s[14:15] offset:1024
	s_mov_b64 exec, -1
	v_and_b32_e32 v77, 16, v76
	v_cmp_ne_u32_e32 vcc, 0, v77
	s_and_b64 exec, exec, vcc
	global_store_dwordx4 v42, v[52:55], s[14:15] offset:2048
	s_mov_b64 exec, -1
	v_and_b32_e32 v77, 64, v76
	v_cmp_ne_u32_e32 vcc, 0, v77
	s_and_b64 exec, exec, vcc
	global_store_dwordx4 v42, v[56:59], s[14:15] offset:3072
	s_mov_b64 exec, -1
	v_and_b32_e32 v77, 256, v76
	v_cmp_ne_u32_e32 vcc, 0, v77
	s_and_b64 exec, exec, vcc
	global_store_dwordx4 v42, v[60:63], s[22:23]
	s_mov_b64 exec, -1
	v_and_b32_e32 v77, 1024, v76
	v_cmp_ne_u32_e32 vcc, 0, v77
	s_and_b64 exec, exec, vcc
	global_store_dwordx4 v42, v[64:67], s[22:23] offset:1024
	s_mov_b64 exec, -1
	v_and_b32_e32 v77, 4096, v76
	v_cmp_ne_u32_e32 vcc, 0, v77
	s_and_b64 exec, exec, vcc
	global_store_dwordx4 v42, v[68:71], s[22:23] offset:2048
	s_mov_b64 exec, -1
	v_and_b32_e32 v77, 16384, v76
	v_cmp_ne_u32_e32 vcc, 0, v77
	s_and_b64 exec, exec, vcc
	global_store_dwordx4 v42, v[72:75], s[22:23] offset:3072
	s_mov_b64 exec, -1
